# speedup vs baseline: 1.0136x; 1.0136x over previous
.LBB0_24:
	s_load_dwordx2 s[4:5], s[0:1], 0x0
	s_ashr_i32 s3, s2, 31
	s_lshl_b64 s[6:7], s[2:3], 15
	v_mov_b32_e32 v1, 0
	s_load_dwordx2 s[0:1], s[0:1], 0x40
	s_waitcnt lgkmcnt(0)
	s_add_u32 s4, s4, s6
	s_addc_u32 s5, s5, s7
	v_lshl_add_u64 v[30:31], v[0:1], 4, s[4:5]
	v_add_co_u32_e32 v10, vcc, 0x1000, v30
	v_lshlrev_b32_e32 v0, 2, v0
	s_nop 0
	v_addc_co_u32_e32 v11, vcc, 0, v31, vcc
	global_load_dwordx4 v[2:5], v[30:31], off nt
	global_load_dwordx4 v[6:9], v[10:11], off nt
	v_add_co_u32_e32 v10, vcc, 0x2000, v30
	v_lshl_or_b32 v42, s2, 13, v0
	s_nop 0
	v_addc_co_u32_e32 v11, vcc, 0, v31, vcc
	v_add_co_u32_e32 v14, vcc, 0x3000, v30
	global_load_dwordx4 v[10:13], v[10:11], off nt
	s_nop 0
	v_addc_co_u32_e32 v15, vcc, 0, v31, vcc
	global_load_dwordx4 v[14:17], v[14:15], off nt
	v_add_co_u32_e32 v18, vcc, 0x4000, v30
	s_mov_b32 s3, 0x24924925
	s_nop 0
	v_addc_co_u32_e32 v19, vcc, 0, v31, vcc
	global_load_dwordx4 v[18:21], v[18:19], off nt
	v_add_co_u32_e32 v22, vcc, 0x5000, v30
	v_lshrrev_b32_e32 v0, 8, v42
	s_nop 0
	v_addc_co_u32_e32 v23, vcc, 0, v31, vcc
	global_load_dwordx4 v[22:25], v[22:23], off nt
	v_add_co_u32_e32 v26, vcc, 0x6000, v30
	v_add_u32_e32 v43, 0x400, v42
	s_nop 0
	v_addc_co_u32_e32 v27, vcc, 0, v31, vcc
	global_load_dwordx4 v[26:29], v[26:27], off nt
	v_add_co_u32_e32 v30, vcc, 0x7000, v30
	v_add_u32_e32 v44, 0x800, v42
	s_nop 0
	v_addc_co_u32_e32 v31, vcc, 0, v31, vcc
	global_load_dwordx4 v[30:33], v[30:31], off nt
	v_add_u32_e32 v45, 0xc00, v42
	v_mul_hi_u32 v0, v0, s3
	v_lshrrev_b32_e32 v34, 8, v43
	v_lshrrev_b32_e32 v35, 8, v44
	s_movk_i32 s4, 0xe80
	v_lshrrev_b32_e32 v36, 8, v45
	v_mul_u32_u24_e32 v46, 0x700, v0
	v_mul_hi_u32 v38, v34, s3
	v_mul_hi_u32 v40, v35, s3
	v_mov_b64_e32 v[34:35], s[0:1]
	v_mul_hi_u32 v47, v36, s3
	v_mul_u32_u24_e32 v48, 0x700, v38
	v_mad_u64_u32 v[36:37], s[0:1], v0, s4, v[34:35]
	v_sub_u32_e32 v0, v42, v46
	v_mul_u32_u24_e32 v49, 0x700, v40
	v_mad_u64_u32 v[38:39], s[0:1], v38, s4, v[34:35]
	v_lshl_add_u64 v[36:37], v[0:1], 1, v[36:37]
	v_sub_u32_e32 v0, v43, v48
	v_mul_u32_u24_e32 v50, 0x700, v47
	v_mad_u64_u32 v[40:41], s[0:1], v40, s4, v[34:35]
	v_lshl_add_u64 v[38:39], v[0:1], 1, v[38:39]
	v_sub_u32_e32 v0, v44, v49
	v_lshl_add_u64 v[40:41], v[0:1], 1, v[40:41]
	v_sub_u32_e32 v0, v45, v50
	s_waitcnt vmcnt(7)
	v_cvt_pk_f16_f32 v5, v4, v5
	v_cvt_pk_f16_f32 v4, v2, v3
	s_waitcnt vmcnt(6)
	v_cvt_pk_f16_f32 v3, v8, v9
	v_cvt_pk_f16_f32 v2, v6, v7
	global_store_dwordx2 v[36:37], v[4:5], off sc0 sc1
	global_store_dwordx2 v[38:39], v[2:3], off sc0 sc1
	v_mad_u64_u32 v[4:5], s[0:1], v47, s4, v[34:35]
	v_lshl_add_u64 v[4:5], v[0:1], 1, v[4:5]
	s_waitcnt vmcnt(7)
	v_cvt_pk_f16_f32 v3, v12, v13
	v_cvt_pk_f16_f32 v2, v10, v11
	global_store_dwordx2 v[40:41], v[2:3], off sc0 sc1
	s_waitcnt vmcnt(7)
	v_cvt_pk_f16_f32 v3, v16, v17
	v_cvt_pk_f16_f32 v2, v14, v15
	v_or_b32_e32 v0, 0x1000, v42
	global_store_dwordx2 v[4:5], v[2:3], off sc0 sc1
	v_lshrrev_b32_e32 v2, 8, v0
	v_mul_hi_u32 v4, v2, s3
	v_mul_u32_u24_e32 v2, 0x700, v4
	v_sub_u32_e32 v0, v0, v2
	v_mad_u64_u32 v[4:5], s[0:1], v4, s4, v[34:35]
	s_waitcnt vmcnt(7)
	v_cvt_pk_f16_f32 v3, v20, v21
	v_cvt_pk_f16_f32 v2, v18, v19
	v_lshl_add_u64 v[4:5], v[0:1], 1, v[4:5]
	v_add_u32_e32 v0, 0x1400, v42
	global_store_dwordx2 v[4:5], v[2:3], off sc0 sc1
	v_lshrrev_b32_e32 v2, 8, v0
	v_mul_hi_u32 v4, v2, s3
	v_mul_u32_u24_e32 v2, 0x700, v4
	v_sub_u32_e32 v0, v0, v2
	v_mad_u64_u32 v[4:5], s[0:1], v4, s4, v[34:35]
	s_waitcnt vmcnt(7)
	v_cvt_pk_f16_f32 v3, v24, v25
	v_cvt_pk_f16_f32 v2, v22, v23
	v_lshl_add_u64 v[4:5], v[0:1], 1, v[4:5]
	v_add_u32_e32 v0, 0x1800, v42
	global_store_dwordx2 v[4:5], v[2:3], off sc0 sc1
	v_lshrrev_b32_e32 v2, 8, v0
	v_mul_hi_u32 v4, v2, s3
	v_mul_u32_u24_e32 v2, 0x700, v4
	v_sub_u32_e32 v0, v0, v2
	v_mad_u64_u32 v[4:5], s[0:1], v4, s4, v[34:35]
	s_waitcnt vmcnt(7)
	v_cvt_pk_f16_f32 v3, v28, v29
	v_cvt_pk_f16_f32 v2, v26, v27
	v_lshl_add_u64 v[4:5], v[0:1], 1, v[4:5]
	v_add_u32_e32 v0, 0x1c00, v42
	global_store_dwordx2 v[4:5], v[2:3], off sc0 sc1
	v_lshrrev_b32_e32 v2, 8, v0
	v_mul_hi_u32 v4, v2, s3
	v_mul_u32_u24_e32 v2, 0x700, v4
	v_sub_u32_e32 v0, v0, v2
	v_mad_u64_u32 v[4:5], s[0:1], v4, s4, v[34:35]
	s_waitcnt vmcnt(7)
	v_cvt_pk_f16_f32 v3, v32, v33
	v_cvt_pk_f16_f32 v2, v30, v31
	v_lshl_add_u64 v[0:1], v[0:1], 1, v[4:5]
	global_store_dwordx2 v[0:1], v[2:3], off sc0 sc1
	s_endpgm
	.p2align	8

.LBB2_37:
	s_and_b64 vcc, exec, s[4:5]
	s_cbranch_vccz .LBB2_46
	s_load_dwordx4 s[4:7], s[0:1], 0x0
	s_load_dwordx4 s[48:51], s[0:1], 0x18
	s_load_dwordx2 s[52:53], s[0:1], 0x10
	s_setprio 3
	s_add_i32 s10, s3, -8
	v_lshrrev_b32_e32 v2, 3, v142
	v_and_b32_e32 v4, 7, v0
	s_lshl_b32 s11, s10, 2
	v_bitop3_b32 v0, v1, v0, 7 bitop3:0x78
	v_mul_u32_u24_e32 v3, 0xe80, v2
	v_bitop3_b32 v2, v1, v4, 4 bitop3:0x36
	s_cmpk_gt_u32 s20, 0x27f
	s_mulk_i32 s21, 0x90
	v_lshl_or_b32 v0, v0, 4, v3
	v_lshl_or_b32 v2, v2, 4, v3
	s_mov_b64 s[0:1], -1
	s_mulk_i32 s19, 0x90
	v_add_u32_e32 v11, s18, v142
	v_lshl_add_u32 v11, s10, 6, v11
	v_and_b32_e32 v11, 0x7ff, v11
	v_lshlrev_b32_e32 v11, 7, v11
	v_min_u32_e32 v12, 4, v142
	v_lshlrev_b32_e32 v12, 7, v12
	v_lshl_add_u32 v12, s21, 2, v12
	s_cbranch_scc0 .LBB2_42
	s_and_b32 s0, s11, 4
	v_bitop3_b32 v5, s0, v4, v1 bitop3:0x36
	s_lshl_b32 s0, s10, 6
	s_add_i32 s0, s0, s18
	s_mul_hi_i32 s1, s0, 0xe80
	s_mulk_i32 s0, 0xe80
	s_waitcnt lgkmcnt(0)
	s_add_u32 s0, s4, s0
	s_addc_u32 s1, s5, s1
	s_lshl_b32 s8, s10, 3
	s_add_i32 s8, s8, s21
	s_mul_hi_u32 s13, s8, 0xe80
	s_mul_i32 s15, s8, 0xe80
	s_lshl_b32 s12, s10, 13
	s_lshl_b32 s14, s10, 10
	s_mov_b32 s8, m0
	s_mov_b32 m0, s12
	s_nop 0
	global_load_lds_dwordx4 v0, s[0:1]
	s_mov_b32 m0, s8
	s_add_u32 s8, s0, 0x7400
	s_addc_u32 s9, s1, 0
	s_add_i32 s16, s12, 0x400
	s_mov_b32 s17, m0
	s_mov_b32 m0, s16
	s_nop 0
	global_load_lds_dwordx4 v2, s[8:9]
	s_mov_b32 m0, s17
	s_add_u32 s8, s0, 0xe800
	s_addc_u32 s9, s1, 0
	s_add_i32 s16, s12, 0x800
	s_mov_b32 s17, m0
	s_mov_b32 m0, s16
	s_nop 0
	global_load_lds_dwordx4 v0, s[8:9]
	s_mov_b32 m0, s17
	s_add_u32 s8, s0, 0x15c00
	s_addc_u32 s9, s1, 0
	s_add_i32 s16, s12, 0xc00
	s_mov_b32 s17, m0
	s_mov_b32 m0, s16
	s_nop 0
	global_load_lds_dwordx4 v2, s[8:9]
	s_mov_b32 m0, s17
	s_add_u32 s8, s0, 0x1d000
	s_addc_u32 s9, s1, 0
	s_add_i32 s16, s12, 0x1000
	s_mov_b32 s17, m0
	s_mov_b32 m0, s16
	s_nop 0
	global_load_lds_dwordx4 v0, s[8:9]
	s_mov_b32 m0, s17
	s_add_u32 s8, s0, 0x24400
	s_addc_u32 s9, s1, 0
	s_add_i32 s16, s12, 0x1400
	s_mov_b32 s17, m0
	s_mov_b32 m0, s16
	s_nop 0
	global_load_lds_dwordx4 v2, s[8:9]
	s_mov_b32 m0, s17
	s_add_u32 s8, s0, 0x2b800
	s_addc_u32 s9, s1, 0
	s_add_i32 s16, s12, 0x1800
	s_mov_b32 s17, m0
	s_mov_b32 m0, s16
	s_nop 0
	global_load_lds_dwordx4 v0, s[8:9]
	s_mov_b32 m0, s17
	s_add_u32 s8, s0, 0x32c00
	s_addc_u32 s9, s1, 0
	s_add_i32 s16, s12, 0x1c00
	s_mov_b32 s17, m0
	s_mov_b32 m0, s16
	s_nop 0
	global_load_lds_dwordx4 v2, s[8:9]
	s_mov_b32 m0, s17
	s_add_u32 s8, s6, s15
	s_addc_u32 s9, s7, s13
	s_add_i32 s13, s14, 0x8000
	v_lshl_or_b32 v5, v5, 4, v3
	s_mov_b32 s15, m0
	s_mov_b32 m0, s13
	s_nop 0
	global_load_lds_dwordx4 v5, s[8:9]
	s_mov_b32 m0, s15
	s_add_u32 s16, s8, 0x1d000
	s_addc_u32 s17, s9, 0
	s_add_i32 s15, s13, 0x1000
	s_mov_b32 s20, m0
	s_mov_b32 m0, s15
	s_nop 0
	global_load_lds_dwordx4 v5, s[16:17]
	s_mov_b32 m0, s20
	s_add_u32 s16, s8, 0x3a000
	s_addc_u32 s17, s9, 0
	s_add_i32 s15, s13, 0x2000
	s_mov_b32 s20, m0
	s_mov_b32 m0, s15
	s_nop 0
	global_load_lds_dwordx4 v5, s[16:17]
	s_mov_b32 m0, s20
	s_add_u32 s16, s8, 0x57000
	s_addc_u32 s17, s9, 0
	s_add_i32 s15, s13, 0x3000
	s_mov_b32 s20, m0
	s_mov_b32 m0, s15
	s_nop 0
	global_load_lds_dwordx4 v5, s[16:17]
	s_mov_b32 m0, s20
	s_add_u32 s16, s0, 0x80
	s_addc_u32 s17, s1, 0
	s_add_i32 s15, s12, 0xc800
	s_mov_b32 s20, m0
	s_mov_b32 m0, s15
	s_nop 0
	global_load_lds_dwordx4 v0, s[16:17]
	s_mov_b32 m0, s20
	s_add_u32 s16, s0, 0x7480
	s_addc_u32 s17, s1, 0
	s_add_i32 s15, s12, 0xcc00
	s_mov_b32 s20, m0
	s_mov_b32 m0, s15
	s_nop 0
	global_load_lds_dwordx4 v2, s[16:17]
	s_mov_b32 m0, s20
	s_add_u32 s16, s0, 0xe880
	s_addc_u32 s17, s1, 0
	s_add_i32 s15, s12, 0xd000
	s_mov_b32 s20, m0
	s_mov_b32 m0, s15
	s_nop 0
	global_load_lds_dwordx4 v0, s[16:17]
	s_mov_b32 m0, s20
	s_add_u32 s16, s0, 0x15c80
	s_addc_u32 s17, s1, 0
	s_add_i32 s15, s12, 0xd400
	s_mov_b32 s20, m0
	s_mov_b32 m0, s15
	s_nop 0
	global_load_lds_dwordx4 v2, s[16:17]
	s_mov_b32 m0, s20
	s_add_u32 s16, s0, 0x1d080
	s_addc_u32 s17, s1, 0
	s_add_i32 s15, s12, 0xd800
	s_mov_b32 s20, m0
	s_mov_b32 m0, s15
	s_nop 0
	global_load_lds_dwordx4 v0, s[16:17]
	s_mov_b32 m0, s20
	s_add_u32 s16, s0, 0x24480
	s_addc_u32 s17, s1, 0
	s_add_i32 s15, s12, 0xdc00
	s_mov_b32 s20, m0
	s_mov_b32 m0, s15
	s_nop 0
	global_load_lds_dwordx4 v2, s[16:17]
	s_mov_b32 m0, s20
	s_add_u32 s16, s0, 0x2b880
	s_addc_u32 s17, s1, 0
	s_add_i32 s15, s12, 0xe000
	s_mov_b32 s20, m0
	s_mov_b32 m0, s15
	s_nop 0
	global_load_lds_dwordx4 v0, s[16:17]
	s_mov_b32 m0, s20
	s_add_u32 s16, s0, 0x32c80
	s_addc_u32 s17, s1, 0
	s_add_i32 s15, s12, 0xe400
	s_mov_b32 s20, m0
	s_mov_b32 m0, s15
	s_nop 0
	global_load_lds_dwordx4 v2, s[16:17]
	s_mov_b32 m0, s20
	s_add_u32 s16, s8, 0x80
	s_addc_u32 s17, s9, 0
	s_add_i32 s15, s14, 0x14800
	s_mov_b32 s20, m0
	s_mov_b32 m0, s15
	s_nop 0
	global_load_lds_dwordx4 v5, s[16:17]
	s_mov_b32 m0, s20
	s_add_u32 s16, s8, 0x1d080
	s_addc_u32 s17, s9, 0
	s_add_i32 s15, s14, 0x15800
	s_mov_b32 s20, m0
	s_mov_b32 m0, s15
	s_nop 0
	global_load_lds_dwordx4 v5, s[16:17]
	s_mov_b32 m0, s20
	s_add_u32 s16, s8, 0x3a080
	s_addc_u32 s17, s9, 0
	s_add_i32 s15, s14, 0x16800
	s_mov_b32 s20, m0
	s_mov_b32 m0, s15
	s_nop 0
	global_load_lds_dwordx4 v5, s[16:17]
	s_mov_b32 m0, s20
	s_add_u32 s16, s8, 0x57080
	s_addc_u32 s17, s9, 0
	s_add_i32 s15, s14, 0x17800
	s_mov_b32 s20, m0
	s_mov_b32 m0, s15
	s_nop 0
	global_load_lds_dwordx4 v5, s[16:17]
	s_mov_b32 m0, s20
	s_add_u32 s16, s0, 0x100
	s_waitcnt vmcnt(12)
	s_barrier
	s_addc_u32 s17, s1, 0
	s_add_i32 s15, s12, 0x19000
	s_mov_b32 s20, m0
	s_mov_b32 m0, s15
	s_nop 0
	global_load_lds_dwordx4 v0, s[16:17]
	s_mov_b32 m0, s20
	s_add_u32 s16, s0, 0x7500
	s_addc_u32 s17, s1, 0
	s_add_i32 s15, s12, 0x19400
	s_mov_b32 s20, m0
	s_mov_b32 m0, s15
	s_nop 0
	global_load_lds_dwordx4 v2, s[16:17]
	s_mov_b32 m0, s20
	s_add_u32 s16, s0, 0xe900
	s_addc_u32 s17, s1, 0
	s_add_i32 s15, s12, 0x19800
	s_mov_b32 s20, m0
	s_mov_b32 m0, s15
	s_nop 0
	global_load_lds_dwordx4 v0, s[16:17]
	s_mov_b32 m0, s20
	s_add_u32 s16, s0, 0x15d00
	s_addc_u32 s17, s1, 0
	s_add_i32 s15, s12, 0x19c00
	s_mov_b32 s20, m0
	s_mov_b32 m0, s15
	s_nop 0
	global_load_lds_dwordx4 v2, s[16:17]
	s_mov_b32 m0, s20
	s_add_u32 s16, s0, 0x1d100
	s_addc_u32 s17, s1, 0
	s_add_i32 s15, s12, 0x1a000
	s_mov_b32 s20, m0
	s_mov_b32 m0, s15
	s_nop 0
	global_load_lds_dwordx4 v0, s[16:17]
	s_mov_b32 m0, s20
	s_add_u32 s16, s0, 0x24500
	s_addc_u32 s17, s1, 0
	s_add_i32 s15, s12, 0x1a400
	s_mov_b32 s20, m0
	s_mov_b32 m0, s15
	s_nop 0
	global_load_lds_dwordx4 v2, s[16:17]
	s_mov_b32 m0, s20
	s_add_u32 s16, s0, 0x2b900
	s_addc_u32 s17, s1, 0
	s_add_i32 s15, s12, 0x1a800
	s_mov_b32 s20, m0
	s_mov_b32 m0, s15
	s_nop 0
	global_load_lds_dwordx4 v0, s[16:17]
	s_mov_b32 m0, s20
	s_add_u32 s16, s0, 0x32d00
	s_addc_u32 s17, s1, 0
	s_add_i32 s15, s12, 0x1ac00
	s_mov_b32 s20, m0
	s_mov_b32 m0, s15
	s_nop 0
	global_load_lds_dwordx4 v2, s[16:17]
	s_mov_b32 m0, s20
	s_add_u32 s16, s8, 0x100
	s_addc_u32 s17, s9, 0
	s_add_i32 s15, s14, 0x21000
	s_mov_b32 s20, m0
	s_mov_b32 m0, s15
	s_nop 0
	global_load_lds_dwordx4 v5, s[16:17]
	s_mov_b32 m0, s20
	s_add_u32 s16, s8, 0x1d100
	s_addc_u32 s17, s9, 0
	s_add_i32 s15, s14, 0x22000
	s_mov_b32 s20, m0
	s_mov_b32 m0, s15
	s_nop 0
	global_load_lds_dwordx4 v5, s[16:17]
	s_mov_b32 m0, s20
	s_add_u32 s16, s8, 0x3a100
	s_addc_u32 s17, s9, 0
	s_add_i32 s15, s14, 0x23000
	s_mov_b32 s20, m0
	s_mov_b32 m0, s15
	s_nop 0
	global_load_lds_dwordx4 v5, s[16:17]
	s_mov_b32 m0, s20
	s_add_u32 s8, s8, 0x57100
	s_addc_u32 s9, s9, 0
	s_add_i32 s14, s14, 0x24000
	s_mov_b32 s15, m0
	s_mov_b32 m0, s14
	s_nop 0
	global_load_lds_dwordx4 v5, s[8:9]
	s_mov_b32 m0, s15
	s_and_b32 s8, s2, 1
	s_mulk_i32 s8, 0x480
	s_add_i32 s8, s8, s19
	s_lshl_b32 s9, s3, 3
	s_add_i32 s8, s8, s9
	s_sub_i32 s8, s8, 64
	s_mul_hi_u32 s9, s8, 0xe80
	s_mulk_i32 s8, 0xe80
	s_add_u32 s14, s6, s8
	s_addc_u32 s15, s7, s9
	s_mov_b32 s16, 0
	s_mov_b64 s[8:9], 0
.LBB2_40:
	s_add_u32 s17, s0, s8
	s_addc_u32 s20, s1, s9
	s_add_i32 s24, s16, s12
	s_add_u32 s22, s17, 0x180
	s_waitcnt vmcnt(12)
	s_barrier
	s_addc_u32 s23, s20, 0
	s_mov_b32 s25, m0
	s_mov_b32 m0, s24
	s_nop 0
	global_load_lds_dwordx4 v0, s[22:23]
	s_mov_b32 m0, s25
	s_add_u32 s22, s17, 0x7580
	s_addc_u32 s23, s20, 0
	s_add_i32 s25, s24, 0x400
	s_mov_b32 s26, m0
	s_mov_b32 m0, s25
	s_nop 0
	global_load_lds_dwordx4 v2, s[22:23]
	s_mov_b32 m0, s26
	s_add_u32 s22, s17, 0xe980
	s_addc_u32 s23, s20, 0
	s_add_i32 s25, s24, 0x800
	s_mov_b32 s26, m0
	s_mov_b32 m0, s25
	s_nop 0
	global_load_lds_dwordx4 v0, s[22:23]
	s_mov_b32 m0, s26
	s_add_u32 s22, s17, 0x15d80
	s_addc_u32 s23, s20, 0
	s_add_i32 s25, s24, 0xc00
	s_mov_b32 s26, m0
	s_mov_b32 m0, s25
	s_nop 0
	global_load_lds_dwordx4 v2, s[22:23]
	s_mov_b32 m0, s26
	s_add_u32 s22, s17, 0x1d180
	s_addc_u32 s23, s20, 0
	s_add_i32 s25, s24, 0x1000
	s_mov_b32 s26, m0
	s_mov_b32 m0, s25
	s_nop 0
	global_load_lds_dwordx4 v0, s[22:23]
	s_mov_b32 m0, s26
	s_add_u32 s22, s17, 0x24580
	s_addc_u32 s23, s20, 0
	s_add_i32 s25, s24, 0x1400
	s_mov_b32 s26, m0
	s_mov_b32 m0, s25
	s_nop 0
	global_load_lds_dwordx4 v2, s[22:23]
	s_mov_b32 m0, s26
	s_add_u32 s22, s17, 0x2b980
	s_addc_u32 s23, s20, 0
	s_add_i32 s25, s24, 0x1800
	s_mov_b32 s26, m0
	s_mov_b32 m0, s25
	s_nop 0
	global_load_lds_dwordx4 v0, s[22:23]
	s_mov_b32 m0, s26
	s_add_u32 s22, s17, 0x32d80
	s_addc_u32 s23, s20, 0
	s_add_i32 s17, s24, 0x1c00
	s_mov_b32 s20, m0
	s_mov_b32 m0, s17
	s_nop 0
	global_load_lds_dwordx4 v2, s[22:23]
	s_mov_b32 m0, s20
	s_add_u32 s17, s14, s8
	s_addc_u32 s20, s15, s9
	s_add_i32 s24, s16, s13
	s_add_u32 s22, s17, 0x180
	s_addc_u32 s23, s20, 0
	s_mov_b32 s25, m0
	s_mov_b32 m0, s24
	s_nop 0
	global_load_lds_dwordx4 v5, s[22:23]
	s_mov_b32 m0, s25
	s_add_u32 s22, s17, 0x1d180
	s_addc_u32 s23, s20, 0
	s_add_i32 s25, s24, 0x1000
	s_mov_b32 s26, m0
	s_mov_b32 m0, s25
	s_nop 0
	global_load_lds_dwordx4 v5, s[22:23]
	s_mov_b32 m0, s26
	s_add_u32 s22, s17, 0x3a180
	s_addc_u32 s23, s20, 0
	s_add_i32 s25, s24, 0x2000
	s_mov_b32 s26, m0
	s_mov_b32 m0, s25
	s_nop 0
	global_load_lds_dwordx4 v5, s[22:23]
	s_mov_b32 m0, s26
	s_add_u32 s22, s17, 0x57180
	s_addc_u32 s23, s20, 0
	s_add_i32 s17, s24, 0x3000
	s_add_i32 s20, s16, 0xc800
	s_cmp_lg_u32 s16, 0x19000
	s_mov_b32 s24, m0
	s_mov_b32 m0, s17
	s_nop 0
	global_load_lds_dwordx4 v5, s[22:23]
	s_mov_b32 m0, s24
	s_cselect_b32 s16, s20, 0
	s_add_u32 s8, s8, 0x80
	s_addc_u32 s9, s9, 0
	s_cmpk_lg_i32 s8, 0xc80
	s_cbranch_scc1 .LBB2_40
	global_load_dword v10, v11, s[48:49]
	global_load_dword v10, v11, s[50:51]
	global_load_dword v10, v12, s[52:53]
	s_waitcnt vmcnt(15)
	s_barrier
	s_waitcnt vmcnt(3)
	s_barrier
	s_mov_b64 s[0:1], 0

.LBB2_44:
	s_add_u32 s7, s0, s2
	s_addc_u32 s12, s1, s3
	s_add_i32 s13, s5, s11
	s_add_u32 s8, s7, 0x180
	s_waitcnt vmcnt(13)
	s_barrier
	s_addc_u32 s9, s12, 0
	s_mov_b32 s14, m0
	s_mov_b32 m0, s13
	s_nop 0
	global_load_lds_dwordx4 v0, s[8:9]
	s_mov_b32 m0, s14
	s_add_u32 s8, s7, 0x7580
	s_addc_u32 s9, s12, 0
	s_add_i32 s14, s13, 0x400
	s_mov_b32 s15, m0
	s_mov_b32 m0, s14
	s_nop 0
	global_load_lds_dwordx4 v2, s[8:9]
	s_mov_b32 m0, s15
	s_add_u32 s8, s7, 0xe980
	s_addc_u32 s9, s12, 0
	s_add_i32 s14, s13, 0x800
	s_mov_b32 s15, m0
	s_mov_b32 m0, s14
	s_nop 0
	global_load_lds_dwordx4 v0, s[8:9]
	s_mov_b32 m0, s15
	s_add_u32 s8, s7, 0x15d80
	s_addc_u32 s9, s12, 0
	s_add_i32 s14, s13, 0xc00
	s_mov_b32 s15, m0
	s_mov_b32 m0, s14
	s_nop 0
	global_load_lds_dwordx4 v2, s[8:9]
	s_mov_b32 m0, s15
	s_add_u32 s8, s7, 0x1d180
	s_addc_u32 s9, s12, 0
	s_add_i32 s14, s13, 0x1000
	s_mov_b32 s15, m0
	s_mov_b32 m0, s14
	s_nop 0
	global_load_lds_dwordx4 v0, s[8:9]
	s_mov_b32 m0, s15
	s_add_u32 s8, s7, 0x24580
	s_addc_u32 s9, s12, 0
	s_add_i32 s14, s13, 0x1400
	s_mov_b32 s15, m0
	s_mov_b32 m0, s14
	s_nop 0
	global_load_lds_dwordx4 v2, s[8:9]
	s_mov_b32 m0, s15
	s_add_u32 s8, s7, 0x2b980
	s_addc_u32 s9, s12, 0
	s_add_i32 s14, s13, 0x1800
	s_mov_b32 s15, m0
	s_mov_b32 m0, s14
	s_nop 0
	global_load_lds_dwordx4 v0, s[8:9]
	s_mov_b32 m0, s15
	s_add_u32 s8, s7, 0x32d80
	s_addc_u32 s9, s12, 0
	s_add_i32 s7, s13, 0x1c00
	s_mov_b32 s12, m0
	s_mov_b32 m0, s7
	s_nop 0
	global_load_lds_dwordx4 v2, s[8:9]
	s_mov_b32 m0, s12
	s_add_u32 s7, s4, s2
	s_addc_u32 s12, s6, s3
	s_add_i32 s13, s5, s10
	s_add_u32 s8, s7, 0x180
	s_addc_u32 s9, s12, 0
	s_mov_b32 s14, m0
	s_mov_b32 m0, s13
	s_nop 0
	global_load_lds_dwordx4 v1, s[8:9]
	s_mov_b32 m0, s14
	s_add_u32 s8, s7, 0x1d180
	s_addc_u32 s9, s12, 0
	s_add_i32 s14, s13, 0x1000
	s_mov_b32 s15, m0
	s_mov_b32 m0, s14
	s_nop 0
	global_load_lds_dwordx4 v1, s[8:9]
	s_mov_b32 m0, s15
	s_add_u32 s8, s7, 0x3a180
	s_addc_u32 s9, s12, 0
	s_add_i32 s14, s13, 0x2000
	s_mov_b32 s15, m0
	s_mov_b32 m0, s14
	s_nop 0
	global_load_lds_dwordx4 v1, s[8:9]
	s_mov_b32 m0, s15
	s_add_u32 s8, s7, 0x57180
	s_addc_u32 s9, s12, 0
	s_add_i32 s14, s13, 0x3000
	s_mov_b32 s15, m0
	s_mov_b32 m0, s14
	s_nop 0
	global_load_lds_dwordx4 v1, s[8:9]
	s_mov_b32 m0, s15
	s_add_u32 s8, s7, 0x74180
	s_addc_u32 s9, s12, 0
	s_add_i32 s7, s13, 0x4000
	s_add_i32 s12, s5, 0xc800
	s_cmp_lg_u32 s5, 0x19000
	s_mov_b32 s13, m0
	s_mov_b32 m0, s7
	s_nop 0
	global_load_lds_dwordx4 v1, s[8:9]
	s_mov_b32 m0, s13
	s_cselect_b32 s5, s12, 0
	s_add_u32 s2, s2, 0x80
	s_addc_u32 s3, s3, 0
	s_cmpk_lg_i32 s2, 0xc80
	s_cbranch_scc1 .LBB2_44
	global_load_dword v10, v11, s[48:49]
	global_load_dword v10, v11, s[50:51]
	global_load_dword v10, v12, s[52:53]
	s_waitcnt vmcnt(16)
	s_barrier
	s_waitcnt vmcnt(3)
	s_barrier

.LBB3_2:
	s_waitcnt lgkmcnt(0)
	s_barrier
	v_add_u32_e32 v104, s14, v31
	ds_read_b128 v[34:37], v104
	ds_read_b128 v[104:107], v104 offset:2048
	v_add_u32_e32 v132, s14, v30
	v_mfma_f32_16x16x32_f16 v[2:5], v[6:9], v[54:57], v[2:5]
	ds_read_b128 v[108:111], v132 offset:32768
	v_mfma_f32_16x16x32_f16 v[10:13], v[6:9], v[26:29], v[10:13]
	v_mfma_f32_16x16x32_f16 v[14:17], v[18:21], v[54:57], v[14:17]
	ds_read_b128 v[112:115], v132 offset:34816
	v_mfma_f32_16x16x32_f16 v[22:25], v[18:21], v[26:29], v[22:25]
	v_mfma_f32_16x16x32_f16 v[38:41], v[42:45], v[54:57], v[38:41]
	ds_read_b128 v[116:119], v132 offset:36864
	v_mfma_f32_16x16x32_f16 v[46:49], v[42:45], v[26:29], v[46:49]
	v_mfma_f32_16x16x32_f16 v[50:53], v[58:61], v[54:57], v[50:53]
	ds_read_b128 v[120:123], v132 offset:38912
	v_mfma_f32_16x16x32_f16 v[62:65], v[58:61], v[26:29], v[62:65]
	v_mfma_f32_16x16x32_f16 v[66:69], v[70:73], v[54:57], v[66:69]
	ds_read_b128 v[124:127], v132 offset:40960
	v_mfma_f32_16x16x32_f16 v[74:77], v[70:73], v[26:29], v[74:77]
	v_mfma_f32_16x16x32_f16 v[78:81], v[82:85], v[54:57], v[78:81]
	ds_read_b128 v[128:131], v132 offset:43008
	v_mfma_f32_16x16x32_f16 v[86:89], v[82:85], v[26:29], v[86:89]
	v_mfma_f32_16x16x32_f16 v[90:93], v[94:97], v[54:57], v[90:93]
	ds_read_b128 v[132:135], v132 offset:45056
	v_mfma_f32_16x16x32_f16 v[98:101], v[94:97], v[26:29], v[98:101]
	v_add_u32_e32 v6, s14, v32
	v_add_u32_e32 v94, s14, v33
	ds_read_b128 v[54:57], v6
	ds_read_b128 v[26:29], v6 offset:2048
	ds_read_b128 v[6:9], v94 offset:32768
	s_waitcnt lgkmcnt(9)
	v_mfma_f32_16x16x32_f16 v[2:5], v[108:111], v[34:37], v[2:5]
	v_mfma_f32_16x16x32_f16 v[10:13], v[108:111], v[104:107], v[10:13]
	ds_read_b128 v[18:21], v94 offset:34816
	s_waitcnt lgkmcnt(9)
	v_mfma_f32_16x16x32_f16 v[14:17], v[112:115], v[34:37], v[14:17]
	v_mfma_f32_16x16x32_f16 v[22:25], v[112:115], v[104:107], v[22:25]
	ds_read_b128 v[42:45], v94 offset:36864
	s_waitcnt lgkmcnt(9)
	v_mfma_f32_16x16x32_f16 v[38:41], v[116:119], v[34:37], v[38:41]
	v_mfma_f32_16x16x32_f16 v[46:49], v[116:119], v[104:107], v[46:49]
	ds_read_b128 v[58:61], v94 offset:38912
	s_waitcnt lgkmcnt(9)
	v_mfma_f32_16x16x32_f16 v[50:53], v[120:123], v[34:37], v[50:53]
	v_mfma_f32_16x16x32_f16 v[62:65], v[120:123], v[104:107], v[62:65]
	ds_read_b128 v[70:73], v94 offset:40960
	s_waitcnt lgkmcnt(9)
	v_mfma_f32_16x16x32_f16 v[66:69], v[124:127], v[34:37], v[66:69]
	v_mfma_f32_16x16x32_f16 v[74:77], v[124:127], v[104:107], v[74:77]
	ds_read_b128 v[82:85], v94 offset:43008
	s_waitcnt lgkmcnt(9)
	v_mfma_f32_16x16x32_f16 v[78:81], v[128:131], v[34:37], v[78:81]
	v_mfma_f32_16x16x32_f16 v[86:89], v[128:131], v[104:107], v[86:89]
	ds_read_b128 v[94:97], v94 offset:45056
	s_waitcnt lgkmcnt(9)
	v_mfma_f32_16x16x32_f16 v[90:93], v[132:135], v[34:37], v[90:93]
	v_mfma_f32_16x16x32_f16 v[98:101], v[132:135], v[104:107], v[98:101]
	s_add_i32 s15, s14, 0xb800
	s_cmp_lg_u32 s14, 0x17000
	s_cselect_b32 s14, s15, 0
	s_add_i32 s13, s13, -1
	s_cmp_eq_u32 s13, 0
	s_cbranch_scc0 .LBB3_2
	s_waitcnt lgkmcnt(6)
	v_mfma_f32_16x16x32_f16 v[30:33], v[6:9], v[54:57], v[2:5]
	v_mfma_f32_16x16x32_f16 v[2:5], v[6:9], v[26:29], v[10:13]
	s_waitcnt lgkmcnt(5)
	v_mfma_f32_16x16x32_f16 v[34:37], v[18:21], v[54:57], v[14:17]
	v_mfma_f32_16x16x32_f16 v[6:9], v[18:21], v[26:29], v[22:25]
	s_waitcnt lgkmcnt(4)
	v_mfma_f32_16x16x32_f16 v[38:41], v[42:45], v[54:57], v[38:41]
	v_mfma_f32_16x16x32_f16 v[10:13], v[42:45], v[26:29], v[46:49]
	s_waitcnt lgkmcnt(3)
	v_mfma_f32_16x16x32_f16 v[42:45], v[58:61], v[54:57], v[50:53]
	v_mfma_f32_16x16x32_f16 v[14:17], v[58:61], v[26:29], v[62:65]
	s_waitcnt lgkmcnt(2)
	v_mfma_f32_16x16x32_f16 v[46:49], v[70:73], v[54:57], v[66:69]
	v_mfma_f32_16x16x32_f16 v[18:21], v[70:73], v[26:29], v[74:77]
	s_waitcnt lgkmcnt(1)
	v_mfma_f32_16x16x32_f16 v[50:53], v[82:85], v[54:57], v[78:81]
	v_mfma_f32_16x16x32_f16 v[22:25], v[82:85], v[26:29], v[86:89]
	s_waitcnt lgkmcnt(0)
	v_mfma_f32_16x16x32_f16 v[54:57], v[94:97], v[54:57], v[90:93]
	v_mfma_f32_16x16x32_f16 v[26:29], v[94:97], v[26:29], v[98:101]
	s_mul_i32 s14, s11, 0x1c0
	s_add_u32 s6, s6, s14
	s_waitcnt lgkmcnt(0)
	s_barrier
	s_addc_u32 s7, s7, 0
	v_lshlrev_b32_e32 v78, 4, v102
	global_load_dwordx4 v[58:61], v78, s[6:7]
	global_load_dwordx4 v[62:65], v78, s[6:7] offset:64
	global_load_dwordx4 v[66:69], v78, s[6:7] offset:128
	global_load_dwordx4 v[70:73], v78, s[6:7] offset:192
	global_load_dwordx4 v[74:77], v78, s[6:7] offset:256
	global_load_dwordx4 v[82:85], v78, s[6:7] offset:320
	global_load_dwordx4 v[86:89], v78, s[6:7] offset:384
	s_mul_i32 s6, s3, 0x3a00
	v_mul_u32_u24_e32 v78, 0x1d0, v103
	v_and_b32_e32 v80, 48, v0
	v_mul_lo_u16_e32 v81, 37, v1
	v_or_b32_e32 v90, 64, v1
	v_add3_u32 v93, s6, v78, v80
	v_lshrrev_b16_e32 v78, 10, v81
	s_or_b32 s12, s12, s9
	v_mul_lo_u16_e32 v80, 0x93, v90
	v_mul_lo_u16_e32 v81, 28, v78
	s_add_u32 s4, s4, s14
	v_mov_b32_e32 v92, 4
	v_lshrrev_b16_e32 v80, 12, v80
	v_sub_u16_e32 v81, v1, v81
	s_addc_u32 s5, s5, 0
	s_movk_i32 s13, 0x1c00
	v_mul_u32_u24_e32 v91, 0x1d0, v78
	v_or_b32_e32 v94, s12, v78
	v_mul_lo_u16_e32 v95, 28, v80
	v_mul_u32_u24_e32 v96, 0x1d0, v80
	v_or_b32_e32 v97, s12, v80
	v_lshlrev_b32_sdwa v78, v92, v81 dst_sel:DWORD dst_unused:UNUSED_PAD src0_sel:DWORD src1_sel:BYTE_0
	v_mov_b64_e32 v[80:81], s[4:5]
	v_mov_b32_e32 v79, 0
	v_sub_u16_e32 v95, v90, v95
	v_add3_u32 v98, s6, v91, v78
	v_mad_i64_i32 v[90:91], s[4:5], v94, s13, v[80:81]
	v_lshl_add_u64 v[90:91], v[90:91], 0, v[78:79]
	v_lshlrev_b32_sdwa v78, v92, v95 dst_sel:DWORD dst_unused:UNUSED_PAD src0_sel:DWORD src1_sel:BYTE_0
	s_movk_i32 s7, 0x1d0
	s_mov_b32 s14, 0x7060302
	s_waitcnt vmcnt(6)
	v_pk_add_f32 v[32:33], v[32:33], v[60:61]
	v_pk_add_f32 v[30:31], v[30:31], v[58:59]
	s_waitcnt vmcnt(5)
	v_pk_add_f32 v[36:37], v[36:37], v[64:65]
	v_pk_add_f32 v[34:35], v[34:35], v[62:63]
	s_waitcnt vmcnt(4)
	v_pk_add_f32 v[40:41], v[40:41], v[68:69]
	v_pk_add_f32 v[38:39], v[38:39], v[66:67]
	s_waitcnt vmcnt(3)
	v_pk_add_f32 v[44:45], v[44:45], v[72:73]
	v_pk_add_f32 v[42:43], v[42:43], v[70:71]
	s_waitcnt vmcnt(2)
	v_pk_add_f32 v[48:49], v[48:49], v[76:77]
	v_pk_add_f32 v[46:47], v[46:47], v[74:75]
	s_waitcnt vmcnt(1)
	v_pk_add_f32 v[52:53], v[52:53], v[84:85]
	v_pk_add_f32 v[50:51], v[50:51], v[82:83]
	s_waitcnt vmcnt(0)
	v_pk_add_f32 v[56:57], v[56:57], v[88:89]
	v_pk_add_f32 v[54:55], v[54:55], v[86:87]
	v_pk_add_f32 v[4:5], v[4:5], v[60:61]
	v_pk_add_f32 v[2:3], v[2:3], v[58:59]
	v_pk_add_f32 v[8:9], v[8:9], v[64:65]
	v_pk_add_f32 v[6:7], v[6:7], v[62:63]
	v_pk_add_f32 v[12:13], v[12:13], v[68:69]
	v_pk_add_f32 v[10:11], v[10:11], v[66:67]
	v_pk_add_f32 v[16:17], v[16:17], v[72:73]
	v_pk_add_f32 v[14:15], v[14:15], v[70:71]
	v_pk_add_f32 v[20:21], v[20:21], v[76:77]
	v_pk_add_f32 v[18:19], v[18:19], v[74:75]
	v_pk_add_f32 v[24:25], v[24:25], v[84:85]
	v_pk_add_f32 v[22:23], v[22:23], v[82:83]
	v_pk_add_f32 v[28:29], v[28:29], v[88:89]
	v_pk_add_f32 v[26:27], v[26:27], v[86:87]
	ds_write_b128 v93, v[30:33]
	ds_write_b128 v93, v[34:37] offset:64
	ds_write_b128 v93, v[38:41] offset:128
	ds_write_b128 v93, v[42:45] offset:192
	ds_write_b128 v93, v[46:49] offset:256
	ds_write_b128 v93, v[50:53] offset:320
	ds_write_b128 v93, v[54:57] offset:384
	ds_write_b128 v93, v[2:5] offset:7424
	ds_write_b128 v93, v[6:9] offset:7488
	ds_write_b128 v93, v[10:13] offset:7552
	ds_write_b128 v93, v[14:17] offset:7616
	ds_write_b128 v93, v[18:21] offset:7680
	ds_write_b128 v93, v[22:25] offset:7744
	ds_write_b128 v93, v[26:29] offset:7808
	s_waitcnt lgkmcnt(0)
	ds_read_b128 v[2:5], v98
	v_add3_u32 v6, s6, v96, v78
	ds_read_b128 v[6:9], v6
	v_mad_i64_i32 v[10:11], s[4:5], v97, s13, v[80:81]
	s_waitcnt lgkmcnt(1)
	global_store_dwordx4 v[90:91], v[2:5], off sc0 sc1
	s_movk_i32 s4, 0xbc
	v_mov_b32_e32 v12, 28
	v_lshl_add_u64 v[2:3], v[10:11], 0, v[78:79]
	s_waitcnt lgkmcnt(0)
	global_store_dwordx4 v[2:3], v[6:9], off sc0 sc1
	v_mov_b32_e32 v2, 0xffffff80
	v_bitop3_b16 v2, v1, s4, v2 bitop3:0xc8
	v_lshrrev_b16_e32 v2, 2, v2
	v_mul_lo_u16_e32 v6, 37, v2
	v_or_b32_e32 v3, 0xffffff80, v1
	v_mul_lo_u16_sdwa v2, v6, v12 dst_sel:DWORD dst_unused:UNUSED_PAD src0_sel:BYTE_1 src1_sel:DWORD
	v_sub_u16_e32 v2, v3, v2
	v_mul_u32_u24_sdwa v3, v6, s7 dst_sel:DWORD dst_unused:UNUSED_PAD src0_sel:BYTE_1 src1_sel:DWORD
	v_or_b32_sdwa v6, s12, v6 dst_sel:DWORD dst_unused:UNUSED_PAD src0_sel:DWORD src1_sel:BYTE_1
	v_lshlrev_b32_sdwa v78, v92, v2 dst_sel:DWORD dst_unused:UNUSED_PAD src0_sel:DWORD src1_sel:BYTE_0
	v_mad_i64_i32 v[6:7], s[4:5], v6, s13, v[80:81]
	v_lshl_add_u64 v[10:11], v[6:7], 0, v[78:79]
	v_or_b32_e32 v6, 0xffffffc0, v1
	v_lshrrev_b16_e32 v7, 2, v6
	v_and_b32_e32 v7, 63, v7
	v_mul_lo_u16_e32 v13, 37, v7
	v_add3_u32 v2, s6, v3, v78
	v_mul_lo_u16_sdwa v7, v13, v12 dst_sel:DWORD dst_unused:UNUSED_PAD src0_sel:BYTE_1 src1_sel:DWORD
	ds_read_b128 v[2:5], v2
	v_sub_u16_e32 v6, v6, v7
	v_mul_u32_u24_sdwa v7, v13, s7 dst_sel:DWORD dst_unused:UNUSED_PAD src0_sel:BYTE_1 src1_sel:DWORD
	v_lshlrev_b32_sdwa v78, v92, v6 dst_sel:DWORD dst_unused:UNUSED_PAD src0_sel:DWORD src1_sel:BYTE_0
	v_add3_u32 v6, s6, v7, v78
	ds_read_b128 v[6:9], v6
	s_waitcnt lgkmcnt(1)
	global_store_dwordx4 v[10:11], v[2:5], off sc0 sc1
	s_nop 1
	v_or_b32_sdwa v2, s12, v13 dst_sel:DWORD dst_unused:UNUSED_PAD src0_sel:DWORD src1_sel:BYTE_1
	v_mad_i64_i32 v[2:3], s[4:5], v2, s13, v[80:81]
	v_lshl_add_u64 v[2:3], v[2:3], 0, v[78:79]
	s_waitcnt lgkmcnt(0)
	global_store_dwordx4 v[2:3], v[6:9], off sc0 sc1
	v_or_b32_e32 v3, 0x100, v1
	v_or_b32_e32 v2, 0x140, v1
	v_mul_u32_u24_e32 v6, 0x925, v3
	v_mul_lo_u16_sdwa v4, v6, v12 dst_sel:DWORD dst_unused:UNUSED_PAD src0_sel:WORD_1 src1_sel:DWORD
	v_sub_u16_e32 v3, v3, v4
	v_mul_u32_u24_e32 v13, 0x925, v2
	v_lshlrev_b32_e32 v78, 4, v3
	v_mul_lo_u16_sdwa v3, v13, v12 dst_sel:DWORD dst_unused:UNUSED_PAD src0_sel:WORD_1 src1_sel:DWORD
	v_sub_u16_e32 v8, v2, v3
	v_perm_b32 v2, v13, v6, s14
	v_pk_mul_lo_u16 v9, v2, s7 op_sel_hi:[1,0]
	v_or_b32_sdwa v6, s12, v6 dst_sel:DWORD dst_unused:UNUSED_PAD src0_sel:DWORD src1_sel:WORD_1
	v_and_b32_e32 v2, 0xfff0, v9
	v_add3_u32 v2, s6, v2, v78
	ds_read_b128 v[2:5], v2
	v_mad_i64_i32 v[6:7], s[4:5], v6, s13, v[80:81]
	v_lshl_add_u64 v[10:11], v[6:7], 0, v[78:79]
	v_lshrrev_b32_e32 v6, 16, v9
	v_lshlrev_b32_e32 v78, 4, v8
	v_add3_u32 v6, s6, v6, v78
	ds_read_b128 v[6:9], v6
	s_waitcnt lgkmcnt(1)
	global_store_dwordx4 v[10:11], v[2:5], off sc0 sc1
	s_nop 1
	v_or_b32_sdwa v2, s12, v13 dst_sel:DWORD dst_unused:UNUSED_PAD src0_sel:DWORD src1_sel:WORD_1
	v_mad_i64_i32 v[2:3], s[4:5], v2, s13, v[80:81]
	v_lshl_add_u64 v[2:3], v[2:3], 0, v[78:79]
	s_waitcnt lgkmcnt(0)
	global_store_dwordx4 v[2:3], v[6:9], off sc0 sc1
	v_or_b32_e32 v3, 0x180, v1
	v_or_b32_e32 v2, 0x1c0, v1
	v_mul_u32_u24_e32 v6, 0x925, v3
	v_mul_lo_u16_sdwa v4, v6, v12 dst_sel:DWORD dst_unused:UNUSED_PAD src0_sel:WORD_1 src1_sel:DWORD
	v_sub_u16_e32 v3, v3, v4
	v_mul_u32_u24_e32 v13, 0x925, v2
	v_lshlrev_b32_e32 v78, 4, v3
	v_mul_lo_u16_sdwa v3, v13, v12 dst_sel:DWORD dst_unused:UNUSED_PAD src0_sel:WORD_1 src1_sel:DWORD
	v_sub_u16_e32 v8, v2, v3
	v_perm_b32 v2, v13, v6, s14
	v_pk_mul_lo_u16 v9, v2, s7 op_sel_hi:[1,0]
	v_or_b32_sdwa v6, s12, v6 dst_sel:DWORD dst_unused:UNUSED_PAD src0_sel:DWORD src1_sel:WORD_1
	v_and_b32_e32 v2, 0xfff0, v9
	v_add3_u32 v2, s6, v2, v78
	ds_read_b128 v[2:5], v2
	v_mad_i64_i32 v[6:7], s[4:5], v6, s13, v[80:81]
	v_lshl_add_u64 v[10:11], v[6:7], 0, v[78:79]
	v_lshrrev_b32_e32 v6, 16, v9
	v_lshlrev_b32_e32 v78, 4, v8
	v_add3_u32 v6, s6, v6, v78
	ds_read_b128 v[6:9], v6
	s_waitcnt lgkmcnt(1)
	global_store_dwordx4 v[10:11], v[2:5], off sc0 sc1
	s_nop 1
	v_or_b32_sdwa v2, s12, v13 dst_sel:DWORD dst_unused:UNUSED_PAD src0_sel:DWORD src1_sel:WORD_1
	v_mad_i64_i32 v[2:3], s[4:5], v2, s13, v[80:81]
	v_lshl_add_u64 v[2:3], v[2:3], 0, v[78:79]
	s_waitcnt lgkmcnt(0)
	global_store_dwordx4 v[2:3], v[6:9], off sc0 sc1
	v_or_b32_e32 v3, 0x200, v1
	v_or_b32_e32 v2, 0x240, v1
	v_mul_u32_u24_e32 v6, 0x925, v3
	v_mul_lo_u16_sdwa v4, v6, v12 dst_sel:DWORD dst_unused:UNUSED_PAD src0_sel:WORD_1 src1_sel:DWORD
	v_sub_u16_e32 v3, v3, v4
	v_mul_u32_u24_e32 v13, 0x925, v2
	v_lshlrev_b32_e32 v78, 4, v3
	v_mul_lo_u16_sdwa v3, v13, v12 dst_sel:DWORD dst_unused:UNUSED_PAD src0_sel:WORD_1 src1_sel:DWORD
	v_sub_u16_e32 v8, v2, v3
	v_perm_b32 v2, v13, v6, s14
	v_pk_mul_lo_u16 v9, v2, s7 op_sel_hi:[1,0]
	v_or_b32_sdwa v6, s12, v6 dst_sel:DWORD dst_unused:UNUSED_PAD src0_sel:DWORD src1_sel:WORD_1
	v_and_b32_e32 v2, 0xfff0, v9
	v_add3_u32 v2, s6, v2, v78
	ds_read_b128 v[2:5], v2
	v_mad_i64_i32 v[6:7], s[4:5], v6, s13, v[80:81]
	v_lshl_add_u64 v[10:11], v[6:7], 0, v[78:79]
	v_lshrrev_b32_e32 v6, 16, v9
	v_lshlrev_b32_e32 v78, 4, v8
	v_add3_u32 v6, s6, v6, v78
	ds_read_b128 v[6:9], v6
	s_waitcnt lgkmcnt(1)
	global_store_dwordx4 v[10:11], v[2:5], off sc0 sc1
	s_nop 1
	v_or_b32_sdwa v2, s12, v13 dst_sel:DWORD dst_unused:UNUSED_PAD src0_sel:DWORD src1_sel:WORD_1
	v_mad_i64_i32 v[2:3], s[4:5], v2, s13, v[80:81]
	v_lshl_add_u64 v[2:3], v[2:3], 0, v[78:79]
	s_waitcnt lgkmcnt(0)
	global_store_dwordx4 v[2:3], v[6:9], off sc0 sc1
	v_or_b32_e32 v3, 0x280, v1
	v_or_b32_e32 v2, 0x2c0, v1
	v_mul_u32_u24_e32 v6, 0x925, v3
	v_mul_lo_u16_sdwa v4, v6, v12 dst_sel:DWORD dst_unused:UNUSED_PAD src0_sel:WORD_1 src1_sel:DWORD
	v_sub_u16_e32 v3, v3, v4
	v_mul_u32_u24_e32 v13, 0x925, v2
	v_lshlrev_b32_e32 v78, 4, v3
	v_mul_lo_u16_sdwa v3, v13, v12 dst_sel:DWORD dst_unused:UNUSED_PAD src0_sel:WORD_1 src1_sel:DWORD
	v_sub_u16_e32 v8, v2, v3
	v_perm_b32 v2, v13, v6, s14
	v_pk_mul_lo_u16 v9, v2, s7 op_sel_hi:[1,0]
	v_or_b32_sdwa v6, s12, v6 dst_sel:DWORD dst_unused:UNUSED_PAD src0_sel:DWORD src1_sel:WORD_1
	v_and_b32_e32 v2, 0xfff0, v9
	v_add3_u32 v2, s6, v2, v78
	ds_read_b128 v[2:5], v2
	v_mad_i64_i32 v[6:7], s[4:5], v6, s13, v[80:81]
	v_lshl_add_u64 v[10:11], v[6:7], 0, v[78:79]
	v_lshrrev_b32_e32 v6, 16, v9
	v_lshlrev_b32_e32 v78, 4, v8
	v_add3_u32 v6, s6, v6, v78
	ds_read_b128 v[6:9], v6
	s_waitcnt lgkmcnt(1)
	global_store_dwordx4 v[10:11], v[2:5], off sc0 sc1
	s_nop 1
	v_or_b32_sdwa v2, s12, v13 dst_sel:DWORD dst_unused:UNUSED_PAD src0_sel:DWORD src1_sel:WORD_1
	v_mad_i64_i32 v[2:3], s[4:5], v2, s13, v[80:81]
	v_lshl_add_u64 v[2:3], v[2:3], 0, v[78:79]
	s_waitcnt lgkmcnt(0)
	global_store_dwordx4 v[2:3], v[6:9], off sc0 sc1
	v_or_b32_e32 v3, 0x300, v1
	v_or_b32_e32 v2, 0x340, v1
	v_mul_u32_u24_e32 v6, 0x925, v3
	v_mul_lo_u16_sdwa v4, v6, v12 dst_sel:DWORD dst_unused:UNUSED_PAD src0_sel:WORD_1 src1_sel:DWORD
	v_sub_u16_e32 v3, v3, v4
	v_mul_u32_u24_e32 v13, 0x925, v2
	v_lshlrev_b32_e32 v78, 4, v3
	v_mul_lo_u16_sdwa v3, v13, v12 dst_sel:DWORD dst_unused:UNUSED_PAD src0_sel:WORD_1 src1_sel:DWORD
	v_sub_u16_e32 v8, v2, v3
	v_perm_b32 v2, v13, v6, s14
	v_pk_mul_lo_u16 v9, v2, s7 op_sel_hi:[1,0]
	v_or_b32_sdwa v6, s12, v6 dst_sel:DWORD dst_unused:UNUSED_PAD src0_sel:DWORD src1_sel:WORD_1
	v_and_b32_e32 v2, 0xfff0, v9
	v_add3_u32 v2, s6, v2, v78
	ds_read_b128 v[2:5], v2
	v_mad_i64_i32 v[6:7], s[4:5], v6, s13, v[80:81]
	v_lshl_add_u64 v[10:11], v[6:7], 0, v[78:79]
	v_lshrrev_b32_e32 v6, 16, v9
	v_lshlrev_b32_e32 v78, 4, v8
	v_add3_u32 v6, s6, v6, v78
	ds_read_b128 v[6:9], v6
	s_waitcnt lgkmcnt(1)
	global_store_dwordx4 v[10:11], v[2:5], off sc0 sc1
	s_nop 1
	v_or_b32_sdwa v2, s12, v13 dst_sel:DWORD dst_unused:UNUSED_PAD src0_sel:DWORD src1_sel:WORD_1
	v_mad_i64_i32 v[2:3], s[4:5], v2, s13, v[80:81]
	v_lshl_add_u64 v[2:3], v[2:3], 0, v[78:79]
	s_mov_b64 s[4:5], 0
	s_waitcnt lgkmcnt(0)
	global_store_dwordx4 v[2:3], v[6:9], off sc0 sc1
